# scan helper waves: cache-warming dword loads for the chunk after next at the end of each chunk; the post-barrier wait leaves those 16 in flight (vmcnt(16)) so the real operand loads hit L2
# baseline (speedup 1.0000x reference)
; __device__ __forceinline__ void scan_unit(Frame& F, const Args& a, int layer, int unit) {
;     ...
;         unsigned long long ph_act = 0ull;
;     ...
;         HELP_LOAD(cur, 0, -2);
;         for (int it = 0; it < NCH + 2; ++it) {
;     ...
;             const unsigned long long ph0 = __builtin_amdgcn_s_memtime();
;     ...
;             HELP_LOAD(nxt, it + 1, it - 1);
;     ...
;             cur = nxt;
;     ...
;             asm volatile("s_waitcnt vmcnt(0) lgkmcnt(0)" ::: "memory"); ph_act += __builtin_amdgcn_s_memtime() - ph0;
;     ...
;             __syncthreads();
;         }
.LBB0_1321:
	s_mov_b64 s[2:3], 0x30000
	s_add_i32 s0, s0, 1
	v_lshl_add_u64 v[44:45], v[44:45], 0, s[2:3]
	s_mov_b64 s[2:3], 0x10000
	v_lshl_add_u64 v[46:47], v[46:47], 0, s[2:3]
	s_mov_b32 s100, 0
	s_add_i32 s101, s0, 3
	s_cmpk_gt_u32 s101, 0x7e
	s_cbranch_scc1 .Lhp_skip
	v_lshl_add_u64 v[224:225], v[44:45], 0, v[42:43]
	v_lshl_add_u64 v[230:231], v[46:47], 0, v[42:43]
	v_add_co_u32_e32 v226, vcc, 0x1a460000, v224
	s_nop 1
	v_addc_co_u32_e32 v227, vcc, 0, v225, vcc
	global_load_dword v204, v[226:227], off
	global_load_dword v204, v[226:227], off offset:2048
	v_add_co_u32_e32 v226, vcc, 0x1a461000, v224
	s_nop 1
	v_addc_co_u32_e32 v227, vcc, 0, v225, vcc
	global_load_dword v204, v[226:227], off
	global_load_dword v204, v[226:227], off offset:2048
	v_add_co_u32_e32 v226, vcc, 0x38420000, v230
	s_nop 1
	v_addc_co_u32_e32 v227, vcc, 0, v231, vcc
	global_load_dword v204, v[226:227], off
	global_load_dword v204, v[226:227], off offset:2048
	v_add_co_u32_e32 v226, vcc, 0x3c420000, v230
	s_nop 1
	v_addc_co_u32_e32 v227, vcc, 0, v231, vcc
	global_load_dword v204, v[226:227], off
	global_load_dword v204, v[226:227], off offset:2048
	v_add_co_u32_e32 v226, vcc, 0x1a462000, v224
	s_nop 1
	v_addc_co_u32_e32 v227, vcc, 0, v225, vcc
	global_load_dword v204, v[226:227], off
	global_load_dword v204, v[226:227], off offset:2048
	v_add_co_u32_e32 v226, vcc, 0x1a463000, v224
	s_nop 1
	v_addc_co_u32_e32 v227, vcc, 0, v225, vcc
	global_load_dword v204, v[226:227], off offset:2048
	v_add_co_u32_e32 v226, vcc, 0x1a464000, v224
	s_nop 1
	v_addc_co_u32_e32 v227, vcc, 0, v225, vcc
	global_load_dword v204, v[226:227], off
	v_add_co_u32_e32 v226, vcc, 0x38421000, v230
	s_nop 1
	v_addc_co_u32_e32 v227, vcc, 0, v231, vcc
	global_load_dword v204, v[226:227], off
	v_add_co_u32_e32 v226, vcc, 0x3c421000, v230
	s_nop 1
	v_addc_co_u32_e32 v227, vcc, 0, v231, vcc
	global_load_dword v204, v[226:227], off
	v_add_co_u32_e32 v226, vcc, 0x1a465000, v224
	s_nop 1
	v_addc_co_u32_e32 v227, vcc, 0, v225, vcc
	global_load_dword v204, v[226:227], off
	s_add_i32 vcc_lo, s0, 2
	s_mov_b32 vcc_hi, 0
	s_lshl_b64 vcc, vcc, 16
	v_lshl_add_u64 v[226:227], v[30:31], 0, vcc
	global_load_dword v204, v[226:227], off
	s_mov_b32 s100, 1
.Lhp_skip:
	s_waitcnt lgkmcnt(0)
	s_barrier
	s_cmp_lg_u32 s100, 0
	s_cbranch_scc1 .Lhp_w16
	s_waitcnt vmcnt(0)
	s_branch .Lhp_wd
.Lhp_w16:
	s_waitcnt vmcnt(16)
.Lhp_wd:
	v_mov_b64_e32 v[20:21], v[4:5]
	v_mov_b64_e32 v[18:19], v[2:3]
	v_mov_b64_e32 v[106:107], v[76:77]
	v_mov_b64_e32 v[96:97], v[74:75]
	v_mov_b64_e32 v[94:95], v[72:73]
	v_mov_b64_e32 v[98:99], v[66:67]
	v_mov_b64_e32 v[104:105], v[64:65]
	v_mov_b64_e32 v[90:91], v[60:61]
	v_mov_b64_e32 v[86:87], v[62:63]
	v_mov_b64_e32 v[92:93], v[68:69]
	v_mov_b64_e32 v[102:103], v[70:71]
	v_mov_b64_e32 v[88:89], v[54:55]
	v_mov_b64_e32 v[84:85], v[56:57]
	v_mov_b64_e32 v[78:79], v[58:59]
	v_mov_b64_e32 v[80:81], v[48:49]
	v_mov_b64_e32 v[100:101], v[50:51]
	v_mov_b64_e32 v[82:83], v[52:53]
	s_cmpk_lg_i32 s0, 0x80
	s_cbranch_scc0 .LBB0_1335
